# combo12 + strategy 4: one static s_setprio 1 for waves 4-7 over the attention phase (reset to 0 at its end)
# baseline (speedup 1.0000x reference)
.LBB0_493:
	s_or_b64 exec, exec, s[24:25]
	s_mov_b32 s0, s61
	s_waitcnt lgkmcnt(0)
	s_barrier
	s_cmp_ge_u32 s61, 4
	s_cbranch_scc0 .Lprio_attn
	s_setprio 1
.Lprio_attn:
	v_mbcnt_lo_u32_b32 v4, -1, 0
	v_mbcnt_hi_u32_b32 v4, -1, v4
	s_nop 0
	v_lshl_or_b32 v0, s0, 6, v4
	s_mov_b32 s0, s61
	s_nop 0
	v_writelane_b32 v254, s0, 58
	s_nop 0
	v_readlane_b32 s4, v254, 7
	v_readlane_b32 s54, v254, 3
	v_readlane_b32 s5, v254, 8
	s_load_dword s0, s[4:5], 0xb0
	s_waitcnt lgkmcnt(0)
	s_load_dwordx2 s[34:35], s[4:5], 0xa8
	v_writelane_b32 v254, s0, 59
	s_movk_i32 s0, 0xc00
	v_cmp_gt_i32_e32 vcc, s0, v0
	s_waitcnt lgkmcnt(0)
	s_barrier
	s_and_saveexec_b64 s[2:3], vcc
	s_cbranch_execz .LBB0_505
	s_load_dwordx2 s[4:5], s[4:5], 0x58
	v_max_i32_e32 v1, 0xa00, v0
	v_sub_u32_e32 v1, v1, v0
	v_readlane_b32 s0, v254, 55
	v_add_u32_e32 v2, 0x1ff, v1
	s_lshl_b32 s0, s0, 2
	v_cmp_lt_u32_e32 vcc, s95, v2
	s_mov_b64 s[8:9], -1
	v_mov_b32_e32 v1, v0
	v_readlane_b32 s1, v254, 56
	s_and_saveexec_b64 s[6:7], vcc
	s_cbranch_execz .LBB0_502
	v_lshrrev_b32_e32 v5, 9, v2
	v_add_u32_e32 v1, 0x200, v0
	v_add_u32_e32 v6, -1, v5
	v_cmp_lt_u32_e32 vcc, 1, v6
	v_mov_b32_e32 v7, 0
	v_mov_b64_e32 v[2:3], v[0:1]
	s_and_saveexec_b64 s[8:9], vcc
	s_cbranch_execz .LBB0_499
	v_lshrrev_b32_e32 v2, 1, v6
	v_add_u32_e32 v2, 1, v2
	s_add_i32 s1, 0, 0xc000
	v_and_b32_e32 v7, -2, v2
	v_lshl_add_u32 v8, v0, 2, s1
	s_mov_b32 s1, 0
	s_mov_b64 s[10:11], 0
	v_mov_b64_e32 v[2:3], v[0:1]

.LBB0_686:
	s_setprio 0
	s_barrier
	s_waitcnt vmcnt(0)
	s_barrier
	v_mbcnt_lo_u32_b32 v0, -1, 0
	v_mbcnt_hi_u32_b32 v0, -1, v0
	s_mov_b32 s0, s61
	s_nop 0
	v_lshl_or_b32 v0, s0, 6, v0
	v_cmp_eq_u32_e32 vcc, 0, v0
	s_and_saveexec_b64 s[24:25], vcc
	s_cbranch_execz .LBB0_730
	v_readlane_b32 s36, v254, 4
	v_readlane_b32 s1, v254, 9
	v_readlane_b32 s37, v254, 5
	v_readlane_b32 s0, v254, 6
	v_mov_b32_e32 v0, s1
	s_waitcnt vmcnt(0) expcnt(0) lgkmcnt(0)
	ds_read_b32 v2, v0
	v_readlane_b32 s1, v254, 10
	s_waitcnt lgkmcnt(0)
	v_cmp_ne_u32_e32 vcc, 0, v2
	v_mov_b32_e32 v0, s1
	ds_read_b32 v0, v0
	s_cbranch_vccnz .LBB0_701
	v_readlane_b32 s2, v254, 0
	v_readlane_b32 s8, v254, 7
	v_readlane_b32 s3, v254, 1
	v_readlane_b32 s9, v254, 8
	s_load_dwordx2 s[6:7], s[2:3], 0x4
	s_load_dword s1, s[8:9], 0xb0
	s_add_u32 s2, s36, 0x1000
	s_addc_u32 s3, s37, 0
	s_add_u32 s4, s36, 0x1100
	s_addc_u32 s5, s37, 0
	s_waitcnt lgkmcnt(0)
	s_mul_i32 s1, s6, s1
	s_add_u32 s6, s36, 0x1200
	s_mul_i32 s1, s1, s7
	s_addc_u32 s7, s37, 0
	s_add_u32 s8, s36, 0x1300
	s_addc_u32 s9, s37, 0
	s_mov_b32 s30, 1
	s_mov_b64 s[10:11], 0
	s_branch .LBB0_691
